# P4: packing of 14 prefetched bf16 values deferred from the top of the unit (where it waited for the just-issued loads) to the take-over, using 6 otherwise unused VGPRs
# speedup vs baseline: 1.0058x; 1.0058x over previous
; #define GAS __attribute__((address_space(1)))
; #define LAS __attribute__((address_space(3)))
; __global__ void __launch_bounds__(NTHR, 2) mk_fwd(Args args) {
;     ...
;                     { const v4u q_ = *(const LAS v4u*)(QGT + lane * 8), g_ = *(const LAS v4u*)(QGT + 512 + lane * 8), t_ = *(const LAS v4u*)(QGT + 1024 + lane * 8);
;                       *(GAS v4u*)(pk + PK_QQ + lane * 16) = q_; *(GAS v4u*)(pk + PK_GG + lane * 16) = g_; *(GAS v4u*)(pk + PK_TT + lane * 16) = t_; }
.LBB0_475:
	s_or_b64 exec, exec, s[34:35]
	s_waitcnt lgkmcnt(0)
	ds_read_b128 v[2:5], v125 offset:10240
	ds_read_b128 v[22:25], v125 offset:11264
	ds_read_b128 v[26:29], v125 offset:12288
	v_add_co_u32_e32 v20, vcc, 0x1000, v20
	s_add_i32 s48, s48, s51
	s_nop 0
	v_addc_co_u32_e32 v21, vcc, 0, v21, vcc
	s_waitcnt lgkmcnt(2)
	global_store_dwordx4 v[20:21], v[2:5], off
	s_waitcnt lgkmcnt(1)
	global_store_dwordx4 v[20:21], v[22:25], off offset:2048
	s_waitcnt lgkmcnt(0)
	global_store_dwordx4 v[20:21], v[26:29], off offset:1024
	s_waitcnt lgkmcnt(0)
	s_andn2_b64 vcc, exec, s[68:69]
	s_waitcnt vmcnt(51)
	v_mov_b32_e32 v57, v160
	s_waitcnt vmcnt(49)
	v_mov_b32_e32 v60, v163
	s_waitcnt vmcnt(47)
	v_mov_b32_e32 v63, v166
	s_waitcnt vmcnt(45)
	v_mov_b32_e32 v66, v169
	s_waitcnt vmcnt(43)
	v_mov_b32_e32 v68, v171
	s_waitcnt vmcnt(41)
	v_mov_b32_e32 v70, v173
	s_waitcnt vmcnt(39)
	v_mov_b32_e32 v72, v175
	s_waitcnt vmcnt(37)
	v_mov_b32_e32 v74, v177
	s_waitcnt vmcnt(35)
	v_mov_b32_e32 v76, v179
	s_waitcnt vmcnt(33)
	v_mov_b32_e32 v78, v181
	s_waitcnt vmcnt(31)
	v_mov_b32_e32 v80, v183
	s_waitcnt vmcnt(29)
	v_mov_b32_e32 v82, v185
	s_waitcnt vmcnt(27)
	v_mov_b32_e32 v84, v187
	s_waitcnt vmcnt(25)
	v_mov_b32_e32 v86, v189
	s_waitcnt vmcnt(23)
	v_mov_b32_e32 v88, v191
	s_waitcnt vmcnt(21)
	v_mov_b32_e32 v90, v193
	v_mov_b32_e32 v58, v162
	v_mov_b32_e32 v62, v165
	v_mov_b32_e32 v65, v168
	v_mov_b32_e32 v67, v170
	v_mov_b32_e32 v69, v172
	v_mov_b32_e32 v71, v174
	v_mov_b32_e32 v73, v176
	v_mov_b32_e32 v75, v178
	v_mov_b32_e32 v77, v180
	v_mov_b32_e32 v79, v182
	v_mov_b32_e32 v81, v184
	v_mov_b32_e32 v83, v186
	v_mov_b32_e32 v85, v188
	v_mov_b32_e32 v87, v190
	v_mov_b32_e32 v89, v192
	v_mov_b32_e32 v91, v196
	v_mov_b32_e32 v20, v127
	v_mov_b32_e32 v23, v130
	v_mov_b32_e32 v41, v146
	v_mov_b32_e32 v21, v126
	v_mov_b32_e32 v22, v129
	v_mov_b32_e32 v26, v132
	v_mov_b32_e32 v30, v134
	v_mov_b32_e32 v31, v136
	v_mov_b32_e32 v34, v138
	v_mov_b32_e32 v35, v140
	v_mov_b32_e32 v37, v142
	v_mov_b32_e32 v39, v144
	v_mov_b32_e32 v44, v147
	v_mov_b32_e32 v46, v149
	v_mov_b32_e32 v48, v151
	v_mov_b32_e32 v50, v153
	v_mov_b32_e32 v52, v155
	v_mov_b32_e32 v54, v157
	v_mov_b32_e32 v56, v159
	v_mov_b32_e32 v61, v164
	v_mov_b32_e32 v24, v128
	v_mov_b32_e32 v25, v131
	v_mov_b32_e32 v27, v133
	v_mov_b32_e32 v29, v135
	v_mov_b32_e32 v32, v137
	v_mov_b32_e32 v33, v139
	v_mov_b32_e32 v36, v141
	v_mov_b32_e32 v38, v143
	v_mov_b32_e32 v43, v145
	v_mov_b32_e32 v45, v148
	v_mov_b32_e32 v47, v150
	v_mov_b32_e32 v49, v152
	v_mov_b32_e32 v51, v154
	v_mov_b32_e32 v53, v156
	v_mov_b32_e32 v55, v158
	v_mov_b32_e32 v59, v161
	v_mov_b32_e32 v64, v167
	s_waitcnt vmcnt(14)
	v_perm_b32 v204, v205, v204, s45
	v_perm_b32 v205, v210, v205, s45
	v_perm_b32 v206, v209, v206, s45
	v_perm_b32 v207, v208, v207, s45
	v_perm_b32 v208, v255, v254, s45
	v_perm_b32 v209, v195, v255, s45
	v_perm_b32 v210, v253, v251, s45
	v_perm_b32 v211, v250, v211, s45
	v_mov_b32_e32 v3, v203
	v_mov_b32_e32 v28, v202
	v_mov_b32_e32 v94, v201
	v_mov_b32_e32 v95, v200
	v_mov_b32_e32 v2, v199
	v_mov_b32_e32 v42, v198
	v_mov_b32_e32 v40, v197
	s_mov_b32 s34, s75
	v_mov_b32_e32 v212, v204
	v_mov_b32_e32 v213, v205
	v_mov_b32_e32 v214, v206
	v_mov_b32_e32 v215, v207
	v_mov_b32_e32 v92, v208
	v_mov_b32_e32 v93, v209
	v_mov_b32_e32 v96, v210
	v_mov_b32_e32 v97, v211
	s_cbranch_vccz .LBB0_480
.LBB0_476:
	s_add_i32 s75, s34, s28
	s_cmpk_gt_i32 s75, 0x3fff
	s_cselect_b64 s[68:69], -1, 0
	s_and_b64 vcc, exec, s[68:69]
	v_mov_b32_e32 v199, v2
	s_cbranch_vccnz .LBB0_478
	s_ashr_i32 s0, s75, 12
	s_bfe_u32 s40, s75, 0x80004
	s_ashr_i32 s1, s0, 31
	s_lshl_b64 s[0:1], s[0:1], 12
	s_lshl_b32 s35, s40, 4
	s_or_b32 s88, s0, s35
	s_add_u32 s43, s88, -1
	s_addc_u32 s64, s1, -1
	s_and_b32 s35, s48, 0x3c0
	s_lshl_b32 s76, s35, 1
	s_cmp_eq_u32 s40, 0
	v_lshl_add_u64 v[4:5], v[14:15], 0, s[76:77]
	s_cselect_b32 s0, s0, s43
	s_cselect_b32 s1, s1, s64
	s_mul_i32 s40, s1, 0x2400
	v_mad_u64_u32 v[130:131], s[0:1], s0, v99, v[4:5]
	v_add_u32_e32 v131, s40, v131
	global_load_ushort v128, v[130:131], off
	global_load_ushort v126, v[130:131], off offset:2048
	v_add_co_u32_e32 v130, vcc, s36, v130
	v_mad_i64_i32 v[4:5], s[0:1], s88, v99, v[4:5]
	s_nop 0
	v_addc_co_u32_e32 v131, vcc, 0, v131, vcc
	v_add_co_u32_e32 v132, vcc, s36, v4
	global_load_ushort v127, v[130:131], off
	s_nop 0
	v_addc_co_u32_e32 v133, vcc, 0, v5, vcc
	global_load_ushort v131, v[4:5], off
	global_load_ushort v129, v[4:5], off offset:2048
	global_load_ushort v130, v[132:133], off
	s_mov_b64 s[0:1], 0x2400
	v_add_co_u32_e32 v132, vcc, s37, v4
	v_lshl_add_u64 v[134:135], v[4:5], 0, s[0:1]
	s_nop 0
	v_addc_co_u32_e32 v133, vcc, 0, v5, vcc
	global_load_ushort v133, v[132:133], off offset:1024
	s_nop 0
	global_load_ushort v132, v[134:135], off offset:2048
	v_add_co_u32_e32 v134, vcc, s38, v4
	s_movk_i32 s40, 0x4000
	s_nop 0
	v_addc_co_u32_e32 v135, vcc, 0, v5, vcc
	global_load_ushort v207, v[134:135], off offset:1024
	s_mov_b64 s[64:65], 0x4800
	v_add_co_u32_e32 v134, vcc, s40, v4
	v_lshl_add_u64 v[136:137], v[4:5], 0, s[64:65]
	s_nop 0
	v_addc_co_u32_e32 v135, vcc, 0, v5, vcc
	s_movk_i32 s0, 0x5000
	global_load_ushort v135, v[134:135], off offset:2048
	s_nop 0
	global_load_ushort v134, v[136:137], off offset:2048
	v_add_co_u32_e32 v136, vcc, s0, v4
	s_movk_i32 s43, 0x6000
	s_nop 0
	v_addc_co_u32_e32 v137, vcc, 0, v5, vcc
	global_load_ushort v208, v[136:137], off offset:2048
	s_mov_b64 s[0:1], 0x6c00
	v_add_co_u32_e32 v136, vcc, s43, v4
	v_lshl_add_u64 v[138:139], v[4:5], 0, s[0:1]
	s_nop 0
	v_addc_co_u32_e32 v137, vcc, 0, v5, vcc
	global_load_ushort v137, v[136:137], off offset:3072
	s_nop 0
	global_load_ushort v136, v[138:139], off offset:2048
	v_add_co_u32_e32 v138, vcc, s42, v4
	s_mov_b64 s[70:71], 0x9000
	s_nop 0
	v_addc_co_u32_e32 v139, vcc, 0, v5, vcc
	v_add_co_u32_e32 v142, vcc, s44, v4
	s_mov_b64 s[0:1], 0xb400
	s_nop 0
	v_addc_co_u32_e32 v143, vcc, 0, v5, vcc
	global_load_ushort v206, v[138:139], off offset:3072
	v_lshl_add_u64 v[140:141], v[4:5], 0, s[70:71]
	global_load_ushort v139, v[142:143], off offset:-4096
	global_load_ushort v138, v[140:141], off offset:2048
	global_load_ushort v209, v[142:143], off
	v_lshl_add_u64 v[142:143], v[4:5], 0, s[0:1]
	s_mov_b32 s0, 0xb000
	v_add_co_u32_e32 v140, vcc, s0, v4
	s_mov_b64 s[80:81], 0xd800
	s_nop 0
	v_addc_co_u32_e32 v141, vcc, 0, v5, vcc
	global_load_ushort v141, v[140:141], off offset:1024
	s_nop 0
	global_load_ushort v140, v[142:143], off offset:2048
	v_add_co_u32_e32 v142, vcc, s39, v4
	v_lshl_add_u64 v[144:145], v[4:5], 0, s[80:81]
	s_nop 0
	v_addc_co_u32_e32 v143, vcc, 0, v5, vcc
	global_load_ushort v204, v[142:143], off offset:1024
	v_add_co_u32_e32 v142, vcc, s41, v4
	s_mov_b32 s0, 0xe000
	s_nop 0
	v_addc_co_u32_e32 v143, vcc, 0, v5, vcc
	global_load_ushort v143, v[142:143], off offset:2048
	s_nop 0
	global_load_ushort v142, v[144:145], off offset:2048
	v_add_co_u32_e32 v144, vcc, s0, v4
	s_mov_b64 s[0:1], 0xfc00
	s_nop 0
	v_addc_co_u32_e32 v145, vcc, 0, v5, vcc
	global_load_ushort v205, v[144:145], off offset:2048
	v_add_co_u32_e32 v144, vcc, s49, v4
	v_lshl_add_u64 v[146:147], v[4:5], 0, s[0:1]
	s_nop 0
	v_addc_co_u32_e32 v145, vcc, 0, v5, vcc
	global_load_ushort v145, v[144:145], off offset:3072
	s_nop 0
	global_load_ushort v144, v[146:147], off offset:2048
	v_add_co_u32_e32 v146, vcc, s50, v4
	s_mov_b64 s[0:1], 0x14400
	s_nop 0
	v_addc_co_u32_e32 v147, vcc, 0, v5, vcc
	v_add_co_u32_e32 v150, vcc, s73, v4
	global_load_ushort v210, v[146:147], off offset:3072
	v_lshl_add_u64 v[146:147], v[4:5], 0, s[46:47]
	v_addc_co_u32_e32 v151, vcc, 0, v5, vcc
	v_lshl_add_u64 v[152:153], v[4:5], 0, s[0:1]
	s_mov_b32 s0, 0x14000
	global_load_ushort v148, v[150:151], off offset:-4096
	s_nop 0
	global_load_ushort v147, v[146:147], off offset:2048
	s_nop 0
	global_load_ushort v146, v[150:151], off
	v_add_co_u32_e32 v150, vcc, s0, v4
	s_mov_b64 s[82:83], 0x16800
	s_nop 0
	v_addc_co_u32_e32 v151, vcc, 0, v5, vcc
	global_load_ushort v150, v[150:151], off offset:1024
	s_nop 0
	global_load_ushort v149, v[152:153], off offset:2048
	v_add_co_u32_e32 v152, vcc, s78, v4
	v_lshl_add_u64 v[154:155], v[4:5], 0, s[82:83]
	s_nop 0
	v_addc_co_u32_e32 v153, vcc, 0, v5, vcc
	global_load_ushort v211, v[152:153], off offset:1024
	v_add_co_u32_e32 v152, vcc, s72, v4
	s_mov_b32 s0, 0x17000
	s_nop 0
	v_addc_co_u32_e32 v153, vcc, 0, v5, vcc
	global_load_ushort v152, v[152:153], off offset:2048
	s_nop 0
	global_load_ushort v151, v[154:155], off offset:2048
	v_add_co_u32_e32 v154, vcc, s0, v4
	s_mov_b64 s[0:1], 0x18c00
	s_nop 0
	v_addc_co_u32_e32 v155, vcc, 0, v5, vcc
	v_lshl_add_u64 v[156:157], v[4:5], 0, s[0:1]
	s_mov_b32 s0, 0x18000
	global_load_ushort v250, v[154:155], off offset:2048
	v_add_co_u32_e32 v154, vcc, s0, v4
	s_mov_b32 s0, 0x19000
	s_nop 0
	v_addc_co_u32_e32 v155, vcc, 0, v5, vcc
	global_load_ushort v154, v[154:155], off offset:3072
	s_nop 0
	global_load_ushort v153, v[156:157], off offset:2048
	v_add_co_u32_e32 v156, vcc, s0, v4
	s_mov_b64 s[0:1], 0x1b000
	s_nop 0
	v_addc_co_u32_e32 v157, vcc, 0, v5, vcc
	v_lshl_add_u64 v[158:159], v[4:5], 0, s[0:1]
	s_mov_b32 s0, 0x1c000
	v_add_co_u32_e32 v160, vcc, s0, v4
	s_mov_b64 s[0:1], 0x1d400
	s_nop 0
	v_addc_co_u32_e32 v161, vcc, 0, v5, vcc
	global_load_ushort v251, v[156:157], off offset:3072
	s_nop 0
	global_load_ushort v156, v[160:161], off offset:-4096
	global_load_ushort v155, v[158:159], off offset:2048
	global_load_ushort v253, v[160:161], off
	v_lshl_add_u64 v[160:161], v[4:5], 0, s[0:1]
	s_mov_b32 s0, 0x1d000
	v_add_co_u32_e32 v158, vcc, s0, v4
	s_mov_b32 s0, 0x1e000
	s_nop 0
	v_addc_co_u32_e32 v159, vcc, 0, v5, vcc
	global_load_ushort v158, v[158:159], off offset:1024
	s_nop 0
	global_load_ushort v157, v[160:161], off offset:2048
	v_add_co_u32_e32 v160, vcc, s0, v4
	s_mov_b64 s[0:1], 0x1f800
	s_nop 0
	v_addc_co_u32_e32 v161, vcc, 0, v5, vcc
	v_lshl_add_u64 v[162:163], v[4:5], 0, s[0:1]
	s_mov_b32 s0, 0x1f000
	global_load_ushort v254, v[160:161], off offset:1024
	v_add_co_u32_e32 v160, vcc, s0, v4
	s_mov_b32 s0, 0x20000
	s_nop 0
	v_addc_co_u32_e32 v161, vcc, 0, v5, vcc
	global_load_ushort v161, v[160:161], off offset:2048
	s_nop 0
	global_load_ushort v159, v[162:163], off offset:2048
	v_add_co_u32_e32 v162, vcc, s0, v4
	s_mov_b64 s[0:1], 0x21c00
	s_nop 0
	v_addc_co_u32_e32 v163, vcc, 0, v5, vcc
	global_load_ushort v255, v[162:163], off offset:2048
	v_lshl_add_u64 v[162:163], v[4:5], 0, s[0:1]
	s_mov_b32 s0, 0x21000
	v_add_co_u32_e32 v164, vcc, s0, v4
	s_mov_b32 s0, 0x22000
	s_nop 0
	v_addc_co_u32_e32 v165, vcc, 0, v5, vcc
	v_add_co_u32_e32 v4, vcc, s0, v4
	global_load_ushort v167, v[164:165], off offset:3072
	s_nop 0
	global_load_ushort v164, v[162:163], off offset:2048
	v_addc_co_u32_e32 v5, vcc, 0, v5, vcc
	global_load_ushort v195, v[4:5], off offset:3072
	v_lshl_add_u64 v[4:5], v[16:17], 0, s[76:77]
	v_mad_i64_i32 v[4:5], s[0:1], s88, v100, v[4:5]
	s_mov_b64 s[0:1], 0x1800
	v_add_co_u32_e32 v170, vcc, s36, v4
	v_lshl_add_u64 v[168:169], v[4:5], 0, s[0:1]
	s_nop 0
	v_addc_co_u32_e32 v171, vcc, 0, v5, vcc
	global_load_ushort v162, v[4:5], off
	global_load_ushort v160, v[4:5], off offset:2048
	global_load_ushort v165, v[170:171], off offset:2048
	global_load_ushort v163, v[168:169], off offset:2048
	s_mov_b64 s[0:1], 0x3000
	v_add_co_u32_e32 v168, vcc, s38, v4
	v_lshl_add_u64 v[170:171], v[4:5], 0, s[0:1]
	s_nop 0
	v_addc_co_u32_e32 v169, vcc, 0, v5, vcc
	global_load_ushort v168, v[168:169], off
	s_nop 0
	global_load_ushort v166, v[170:171], off offset:2048
	v_add_co_u32_e32 v170, vcc, s40, v4
	v_lshl_add_u64 v[172:173], v[4:5], 0, s[64:65]
	s_nop 0
	v_addc_co_u32_e32 v171, vcc, 0, v5, vcc
	global_load_ushort v170, v[170:171], off offset:2048
	s_nop 0
	global_load_ushort v169, v[172:173], off offset:2048
	s_mov_b64 s[0:1], 0x6000
	v_add_co_u32_e32 v172, vcc, s43, v4
	v_lshl_add_u64 v[174:175], v[4:5], 0, s[0:1]
	s_nop 0
	v_addc_co_u32_e32 v173, vcc, 0, v5, vcc
	global_load_ushort v172, v[172:173], off
	s_nop 0
	global_load_ushort v171, v[174:175], off offset:2048
	s_mov_b64 s[0:1], 0x7800
	v_add_co_u32_e32 v174, vcc, s42, v4
	v_lshl_add_u64 v[176:177], v[4:5], 0, s[0:1]
	s_nop 0
	v_addc_co_u32_e32 v175, vcc, 0, v5, vcc
	s_mov_b32 s0, 0x9000
	global_load_ushort v174, v[174:175], off offset:2048
	s_nop 0
	global_load_ushort v173, v[176:177], off offset:2048
	v_add_co_u32_e32 v176, vcc, s0, v4
	v_lshl_add_u64 v[178:179], v[4:5], 0, s[70:71]
	s_nop 0
	v_addc_co_u32_e32 v177, vcc, 0, v5, vcc
	global_load_ushort v176, v[176:177], off
	s_nop 0
	global_load_ushort v175, v[178:179], off offset:2048
	s_mov_b64 s[0:1], 0xa800
	v_add_co_u32_e32 v178, vcc, s44, v4
	v_lshl_add_u64 v[180:181], v[4:5], 0, s[0:1]
	s_nop 0
	v_addc_co_u32_e32 v179, vcc, 0, v5, vcc
	global_load_ushort v178, v[178:179], off offset:2048
	s_nop 0
	global_load_ushort v177, v[180:181], off offset:2048
	s_mov_b64 s[0:1], 0xc000
	v_add_co_u32_e32 v180, vcc, s39, v4
	v_lshl_add_u64 v[182:183], v[4:5], 0, s[0:1]
	s_nop 0
	v_addc_co_u32_e32 v181, vcc, 0, v5, vcc
	global_load_ushort v180, v[180:181], off
	s_nop 0
	global_load_ushort v179, v[182:183], off offset:2048
	v_add_co_u32_e32 v182, vcc, s41, v4
	v_lshl_add_u64 v[184:185], v[4:5], 0, s[80:81]
	s_nop 0
	v_addc_co_u32_e32 v183, vcc, 0, v5, vcc
	global_load_ushort v182, v[182:183], off offset:2048
	s_nop 0
	global_load_ushort v181, v[184:185], off offset:2048
	s_mov_b64 s[0:1], 0xf000
	v_add_co_u32_e32 v184, vcc, s49, v4
	v_lshl_add_u64 v[186:187], v[4:5], 0, s[0:1]
	s_nop 0
	v_addc_co_u32_e32 v185, vcc, 0, v5, vcc
	global_load_ushort v184, v[184:185], off
	s_nop 0
	global_load_ushort v183, v[186:187], off offset:2048
	s_mov_b64 s[0:1], 0x10800
	v_add_co_u32_e32 v186, vcc, s50, v4
	v_lshl_add_u64 v[188:189], v[4:5], 0, s[0:1]
	s_nop 0
	v_addc_co_u32_e32 v187, vcc, 0, v5, vcc
	s_mov_b32 s0, 0x12000
	global_load_ushort v186, v[186:187], off offset:2048
	s_nop 0
	global_load_ushort v185, v[188:189], off offset:2048
	v_add_co_u32_e32 v188, vcc, s0, v4
	v_lshl_add_u64 v[190:191], v[4:5], 0, s[46:47]
	s_nop 0
	v_addc_co_u32_e32 v189, vcc, 0, v5, vcc
	global_load_ushort v188, v[188:189], off
	s_nop 0
	global_load_ushort v187, v[190:191], off offset:2048
	s_mov_b64 s[0:1], 0x13800
	v_add_co_u32_e32 v190, vcc, s73, v4
	v_lshl_add_u64 v[192:193], v[4:5], 0, s[0:1]
	s_nop 0
	v_addc_co_u32_e32 v191, vcc, 0, v5, vcc
	global_load_ushort v190, v[190:191], off offset:2048
	s_nop 0
	global_load_ushort v189, v[192:193], off offset:2048
	v_add_co_u32_e32 v192, vcc, s78, v4
	s_mov_b64 s[0:1], 0x15000
	s_nop 0
	v_addc_co_u32_e32 v193, vcc, 0, v5, vcc
	v_lshl_add_u64 v[196:197], v[4:5], 0, s[0:1]
	v_lshl_add_u64 v[198:199], v[4:5], 0, s[82:83]
	v_add_co_u32_e32 v4, vcc, s72, v4
	global_load_ushort v192, v[192:193], off
	s_nop 0
	global_load_ushort v191, v[196:197], off offset:2048
	v_addc_co_u32_e32 v5, vcc, 0, v5, vcc
	global_load_ushort v196, v[4:5], off offset:2048
	global_load_ushort v193, v[198:199], off offset:2048
	v_or_b32_e32 v4, s35, v194
	v_readlane_b32 s80, v252, 0
	v_lshlrev_b32_e32 v4, 2, v4
	v_mov_b32_e32 v5, v7
	v_readlane_b32 s84, v252, 4
	v_readlane_b32 s85, v252, 5
	v_readlane_b32 s86, v252, 6
	v_readlane_b32 s87, v252, 7
	v_lshl_add_u64 v[200:201], s[84:85], 0, v[4:5]
	v_add_co_u32_e32 v198, vcc, s36, v200
	v_readlane_b32 s90, v252, 10
	s_nop 0
	v_addc_co_u32_e32 v199, vcc, 0, v201, vcc
	v_add_co_u32_e32 v200, vcc, 0x2000, v200
	v_readlane_b32 s91, v252, 11
	s_nop 0
	v_addc_co_u32_e32 v201, vcc, 0, v201, vcc
	global_load_dword v197, v4, s[84:85]
	global_load_dword v198, v[198:199], off
	s_nop 0
	global_load_dword v199, v[200:201], off
	s_nop 0
	global_load_dword v200, v4, s[86:87]
	global_load_dword v201, v4, s[90:91]
	global_load_dword v202, v4, s[52:53]
	global_load_dword v203, v4, s[54:55]
	v_readlane_b32 s81, v252, 1
	v_readlane_b32 s82, v252, 2
	v_readlane_b32 s83, v252, 3
	v_readlane_b32 s88, v252, 8
	v_readlane_b32 s89, v252, 9
	v_readlane_b32 s92, v252, 12
	v_readlane_b32 s93, v252, 13
	v_readlane_b32 s94, v252, 14
	v_readlane_b32 s95, v252, 15

; __global__ void __launch_bounds__(NTHR, 2) mk_fwd(Args args) {
;     ...
;                 }
;             }
;     }
.LBB0_480:
	v_lshlrev_b32_e32 v195, 2, v0
	v_readlane_b32 s88, v252, 44
	v_readlane_b32 s78, v252, 50
	v_readlane_b32 s2, v252, 52
	v_readlane_b32 s89, v252, 45
	v_readlane_b32 s79, v252, 51
	v_readlane_b32 s3, v252, 53

; __global__ void __launch_bounds__(NTHR, 2) mk_fwd(Args args) {
	.amdhsa_kernel _Z6mk_fwd4Args
		.amdhsa_group_segment_fixed_size 0
		.amdhsa_private_segment_fixed_size 0
		.amdhsa_kernarg_size 496
		.amdhsa_user_sgpr_count 2
		.amdhsa_user_sgpr_dispatch_ptr 0
		.amdhsa_user_sgpr_queue_ptr 0
		.amdhsa_user_sgpr_kernarg_segment_ptr 1
		.amdhsa_user_sgpr_dispatch_id 0
		.amdhsa_user_sgpr_kernarg_preload_length 0
		.amdhsa_user_sgpr_kernarg_preload_offset 0
		.amdhsa_user_sgpr_private_segment_size 0
		.amdhsa_uses_dynamic_stack 0
		.amdhsa_enable_private_segment 0
		.amdhsa_system_sgpr_workgroup_id_x 1
		.amdhsa_system_sgpr_workgroup_id_y 0
		.amdhsa_system_sgpr_workgroup_id_z 0
		.amdhsa_system_sgpr_workgroup_info 0
		.amdhsa_system_vgpr_workitem_id 0
		.amdhsa_next_free_vgpr 256
		.amdhsa_next_free_sgpr 100
		.amdhsa_accum_offset 256
		.amdhsa_reserve_vcc 1
		.amdhsa_float_round_mode_32 0
		.amdhsa_float_round_mode_16_64 0
		.amdhsa_float_denorm_mode_32 3
		.amdhsa_float_denorm_mode_16_64 3
		.amdhsa_dx10_clamp 1
		.amdhsa_ieee_mode 1
		.amdhsa_fp16_overflow 0
		.amdhsa_tg_split 0
		.amdhsa_exception_fp_ieee_invalid_op 0
		.amdhsa_exception_fp_denorm_src 0
		.amdhsa_exception_fp_ieee_div_zero 0
		.amdhsa_exception_fp_ieee_overflow 0
		.amdhsa_exception_fp_ieee_underflow 0
		.amdhsa_exception_fp_ieee_inexact 0
		.amdhsa_exception_int_div_zero 0
	.end_amdhsa_kernel

; __global__ void __launch_bounds__(NTHR, 2) mk_fwd(Args args) {
.Lfunc_end0:
	.size	_Z6mk_fwd4Args, .Lfunc_end0-_Z6mk_fwd4Args
	.set _Z6mk_fwd4Args.num_vgpr, 256
	.set _Z6mk_fwd4Args.num_agpr, 0
	.set _Z6mk_fwd4Args.numbered_sgpr, 100
	.set _Z6mk_fwd4Args.num_named_barrier, 0
	.set _Z6mk_fwd4Args.private_seg_size, 0
	.set _Z6mk_fwd4Args.uses_vcc, 1
	.set _Z6mk_fwd4Args.uses_flat_scratch, 0
	.set _Z6mk_fwd4Args.has_dyn_sized_stack, 0
	.set _Z6mk_fwd4Args.has_recursion, 0
	.set _Z6mk_fwd4Args.has_indirect_call, 0

; __global__ void __launch_bounds__(NTHR, 2) mk_fwd(Args args) {
amdhsa.kernels:
  - .agpr_count:     0
    .args:
      - .offset:         0
        .size:           240
        .value_kind:     by_value
      - .offset:         240
        .size:           4
        .value_kind:     hidden_block_count_x
      - .offset:         244
        .size:           4
        .value_kind:     hidden_block_count_y
      - .offset:         248
        .size:           4
        .value_kind:     hidden_block_count_z
      - .offset:         252
        .size:           2
        .value_kind:     hidden_group_size_x
      - .offset:         254
        .size:           2
        .value_kind:     hidden_group_size_y
      - .offset:         256
        .size:           2
        .value_kind:     hidden_group_size_z
      - .offset:         258
        .size:           2
        .value_kind:     hidden_remainder_x
      - .offset:         260
        .size:           2
        .value_kind:     hidden_remainder_y
      - .offset:         262
        .size:           2
        .value_kind:     hidden_remainder_z
      - .offset:         280
        .size:           8
        .value_kind:     hidden_global_offset_x
      - .offset:         288
        .size:           8
        .value_kind:     hidden_global_offset_y
      - .offset:         296
        .size:           8
        .value_kind:     hidden_global_offset_z
      - .offset:         304
        .size:           2
        .value_kind:     hidden_grid_dims
      - .offset:         360
        .size:           4
        .value_kind:     hidden_dynamic_lds_size
    .group_segment_fixed_size: 0
    .kernarg_segment_align: 8
    .kernarg_segment_size: 496
    .language:       OpenCL C
    .language_version:
      - 2
      - 0
    .max_flat_workgroup_size: 512
    .name:           _Z6mk_fwd4Args
    .private_segment_fixed_size: 0
    .sgpr_count:     106
    .sgpr_spill_count: 54
    .symbol:         _Z6mk_fwd4Args.kd
    .uniform_work_group_size: 1
    .uses_dynamic_stack: false
    .vgpr_count:     256
    .vgpr_spill_count: 0
    .wavefront_size: 64
